# gate/up GEMM epilogue: swiglu computed in batches of 8 independent elements (no dependent-chain stalls or trans hazard nops), addresses from one base
# speedup vs baseline: 1.0056x; 1.0010x over previous
.LBB0_1331:
	v_lshl_add_u32 v174, s30, 8, v153
	v_lshl_or_b32 v176, s29, 7, v141
	v_ashrrev_i32_e32 v175, 31, v174
	v_ashrrev_i32_e32 v177, 31, v176
	v_lshlrev_b64 v[174:175], 12, v[174:175]
	v_lshlrev_b64 v[176:177], 1, v[176:177]
	v_lshl_add_u64 v[174:175], s[44:45], 0, v[174:175]
	v_lshl_add_u64 v[178:179], v[174:175], 0, v[176:177]
	v_mul_f32_e32 v160, 0xbfb8aa3b, v126
	v_mul_f32_e32 v161, 0xbfb8aa3b, v127
	v_mul_f32_e32 v162, 0xbfb8aa3b, v128
	v_mul_f32_e32 v163, 0xbfb8aa3b, v129
	v_mul_f32_e32 v164, 0xbfb8aa3b, v118
	v_mul_f32_e32 v165, 0xbfb8aa3b, v119
	v_mul_f32_e32 v166, 0xbfb8aa3b, v120
	v_mul_f32_e32 v167, 0xbfb8aa3b, v121
	v_exp_f32_e32 v160, v160
	v_exp_f32_e32 v161, v161
	v_exp_f32_e32 v162, v162
	v_exp_f32_e32 v163, v163
	v_exp_f32_e32 v164, v164
	v_exp_f32_e32 v165, v165
	v_exp_f32_e32 v166, v166
	v_exp_f32_e32 v167, v167
	v_add_f32_e32 v160, 1.0, v160
	v_add_f32_e32 v161, 1.0, v161
	v_add_f32_e32 v162, 1.0, v162
	v_add_f32_e32 v163, 1.0, v163
	v_add_f32_e32 v164, 1.0, v164
	v_add_f32_e32 v165, 1.0, v165
	v_add_f32_e32 v166, 1.0, v166
	v_add_f32_e32 v167, 1.0, v167
	v_rcp_f32_e32 v160, v160
	v_rcp_f32_e32 v161, v161
	v_rcp_f32_e32 v162, v162
	v_rcp_f32_e32 v163, v163
	v_rcp_f32_e32 v164, v164
	v_rcp_f32_e32 v165, v165
	v_rcp_f32_e32 v166, v166
	v_rcp_f32_e32 v167, v167
	v_mul_f32_e32 v160, v126, v160
	v_mul_f32_e32 v161, v127, v161
	v_mul_f32_e32 v162, v128, v162
	v_mul_f32_e32 v163, v129, v163
	v_mul_f32_e32 v164, v118, v164
	v_mul_f32_e32 v165, v119, v165
	v_mul_f32_e32 v166, v120, v166
	v_mul_f32_e32 v167, v121, v167
	v_mul_f32_e32 v160, v160, v122
	v_mul_f32_e32 v161, v161, v123
	v_mul_f32_e32 v162, v162, v124
	v_mul_f32_e32 v163, v163, v125
	v_mul_f32_e32 v164, v164, v114
	v_mul_f32_e32 v165, v165, v115
	v_mul_f32_e32 v166, v166, v116
	v_mul_f32_e32 v167, v167, v117
	v_cvt_pk_bf16_f32 v168, v160, v161
	v_cvt_pk_bf16_f32 v169, v162, v163
	v_cvt_pk_bf16_f32 v170, v164, v165
	v_cvt_pk_bf16_f32 v171, v166, v167
	global_store_dwordx4 v[178:179], v[168:171], off
	v_mul_f32_e32 v160, 0xbfb8aa3b, v110
	v_mul_f32_e32 v161, 0xbfb8aa3b, v111
	v_mul_f32_e32 v162, 0xbfb8aa3b, v112
	v_mul_f32_e32 v163, 0xbfb8aa3b, v113
	v_mul_f32_e32 v164, 0xbfb8aa3b, v102
	v_mul_f32_e32 v165, 0xbfb8aa3b, v103
	v_mul_f32_e32 v166, 0xbfb8aa3b, v104
	v_mul_f32_e32 v167, 0xbfb8aa3b, v105
	v_exp_f32_e32 v160, v160
	v_exp_f32_e32 v161, v161
	v_exp_f32_e32 v162, v162
	v_exp_f32_e32 v163, v163
	v_exp_f32_e32 v164, v164
	v_exp_f32_e32 v165, v165
	v_exp_f32_e32 v166, v166
	v_exp_f32_e32 v167, v167
	v_add_f32_e32 v160, 1.0, v160
	v_add_f32_e32 v161, 1.0, v161
	v_add_f32_e32 v162, 1.0, v162
	v_add_f32_e32 v163, 1.0, v163
	v_add_f32_e32 v164, 1.0, v164
	v_add_f32_e32 v165, 1.0, v165
	v_add_f32_e32 v166, 1.0, v166
	v_add_f32_e32 v167, 1.0, v167
	v_rcp_f32_e32 v160, v160
	v_rcp_f32_e32 v161, v161
	v_rcp_f32_e32 v162, v162
	v_rcp_f32_e32 v163, v163
	v_rcp_f32_e32 v164, v164
	v_rcp_f32_e32 v165, v165
	v_rcp_f32_e32 v166, v166
	v_rcp_f32_e32 v167, v167
	v_mul_f32_e32 v160, v110, v160
	v_mul_f32_e32 v161, v111, v161
	v_mul_f32_e32 v162, v112, v162
	v_mul_f32_e32 v163, v113, v163
	v_mul_f32_e32 v164, v102, v164
	v_mul_f32_e32 v165, v103, v165
	v_mul_f32_e32 v166, v104, v166
	v_mul_f32_e32 v167, v105, v167
	v_mul_f32_e32 v160, v160, v106
	v_mul_f32_e32 v161, v161, v107
	v_mul_f32_e32 v162, v162, v108
	v_mul_f32_e32 v163, v163, v109
	v_mul_f32_e32 v164, v164, v98
	v_mul_f32_e32 v165, v165, v99
	v_mul_f32_e32 v166, v166, v100
	v_mul_f32_e32 v167, v167, v101
	v_add_co_u32_e32 v172, vcc, 0x10000, v178
	v_cvt_pk_bf16_f32 v168, v160, v161
	v_cvt_pk_bf16_f32 v169, v162, v163
	v_cvt_pk_bf16_f32 v170, v164, v165
	v_cvt_pk_bf16_f32 v171, v166, v167
	v_addc_co_u32_e32 v173, vcc, 0, v179, vcc
	global_store_dwordx4 v[172:173], v[168:171], off
	v_mul_f32_e32 v160, 0xbfb8aa3b, v94
	v_mul_f32_e32 v161, 0xbfb8aa3b, v95
	v_mul_f32_e32 v162, 0xbfb8aa3b, v96
	v_mul_f32_e32 v163, 0xbfb8aa3b, v97
	v_mul_f32_e32 v164, 0xbfb8aa3b, v86
	v_mul_f32_e32 v165, 0xbfb8aa3b, v87
	v_mul_f32_e32 v166, 0xbfb8aa3b, v88
	v_mul_f32_e32 v167, 0xbfb8aa3b, v89
	v_exp_f32_e32 v160, v160
	v_exp_f32_e32 v161, v161
	v_exp_f32_e32 v162, v162
	v_exp_f32_e32 v163, v163
	v_exp_f32_e32 v164, v164
	v_exp_f32_e32 v165, v165
	v_exp_f32_e32 v166, v166
	v_exp_f32_e32 v167, v167
	v_add_f32_e32 v160, 1.0, v160
	v_add_f32_e32 v161, 1.0, v161
	v_add_f32_e32 v162, 1.0, v162
	v_add_f32_e32 v163, 1.0, v163
	v_add_f32_e32 v164, 1.0, v164
	v_add_f32_e32 v165, 1.0, v165
	v_add_f32_e32 v166, 1.0, v166
	v_add_f32_e32 v167, 1.0, v167
	v_rcp_f32_e32 v160, v160
	v_rcp_f32_e32 v161, v161
	v_rcp_f32_e32 v162, v162
	v_rcp_f32_e32 v163, v163
	v_rcp_f32_e32 v164, v164
	v_rcp_f32_e32 v165, v165
	v_rcp_f32_e32 v166, v166
	v_rcp_f32_e32 v167, v167
	v_mul_f32_e32 v160, v94, v160
	v_mul_f32_e32 v161, v95, v161
	v_mul_f32_e32 v162, v96, v162
	v_mul_f32_e32 v163, v97, v163
	v_mul_f32_e32 v164, v86, v164
	v_mul_f32_e32 v165, v87, v165
	v_mul_f32_e32 v166, v88, v166
	v_mul_f32_e32 v167, v89, v167
	v_mul_f32_e32 v160, v160, v90
	v_mul_f32_e32 v161, v161, v91
	v_mul_f32_e32 v162, v162, v92
	v_mul_f32_e32 v163, v163, v93
	v_mul_f32_e32 v164, v164, v82
	v_mul_f32_e32 v165, v165, v83
	v_mul_f32_e32 v166, v166, v84
	v_mul_f32_e32 v167, v167, v85
	v_add_co_u32_e32 v172, vcc, 0x20000, v178
	v_cvt_pk_bf16_f32 v168, v160, v161
	v_cvt_pk_bf16_f32 v169, v162, v163
	v_cvt_pk_bf16_f32 v170, v164, v165
	v_cvt_pk_bf16_f32 v171, v166, v167
	v_addc_co_u32_e32 v173, vcc, 0, v179, vcc
	global_store_dwordx4 v[172:173], v[168:171], off
	v_mul_f32_e32 v160, 0xbfb8aa3b, v78
	v_mul_f32_e32 v161, 0xbfb8aa3b, v79
	v_mul_f32_e32 v162, 0xbfb8aa3b, v80
	v_mul_f32_e32 v163, 0xbfb8aa3b, v81
	v_mul_f32_e32 v164, 0xbfb8aa3b, v70
	v_mul_f32_e32 v165, 0xbfb8aa3b, v71
	v_mul_f32_e32 v166, 0xbfb8aa3b, v72
	v_mul_f32_e32 v167, 0xbfb8aa3b, v73
	v_exp_f32_e32 v160, v160
	v_exp_f32_e32 v161, v161
	v_exp_f32_e32 v162, v162
	v_exp_f32_e32 v163, v163
	v_exp_f32_e32 v164, v164
	v_exp_f32_e32 v165, v165
	v_exp_f32_e32 v166, v166
	v_exp_f32_e32 v167, v167
	v_add_f32_e32 v160, 1.0, v160
	v_add_f32_e32 v161, 1.0, v161
	v_add_f32_e32 v162, 1.0, v162
	v_add_f32_e32 v163, 1.0, v163
	v_add_f32_e32 v164, 1.0, v164
	v_add_f32_e32 v165, 1.0, v165
	v_add_f32_e32 v166, 1.0, v166
	v_add_f32_e32 v167, 1.0, v167
	v_rcp_f32_e32 v160, v160
	v_rcp_f32_e32 v161, v161
	v_rcp_f32_e32 v162, v162
	v_rcp_f32_e32 v163, v163
	v_rcp_f32_e32 v164, v164
	v_rcp_f32_e32 v165, v165
	v_rcp_f32_e32 v166, v166
	v_rcp_f32_e32 v167, v167
	v_mul_f32_e32 v160, v78, v160
	v_mul_f32_e32 v161, v79, v161
	v_mul_f32_e32 v162, v80, v162
	v_mul_f32_e32 v163, v81, v163
	v_mul_f32_e32 v164, v70, v164
	v_mul_f32_e32 v165, v71, v165
	v_mul_f32_e32 v166, v72, v166
	v_mul_f32_e32 v167, v73, v167
	v_mul_f32_e32 v160, v160, v74
	v_mul_f32_e32 v161, v161, v75
	v_mul_f32_e32 v162, v162, v76
	v_mul_f32_e32 v163, v163, v77
	v_mul_f32_e32 v164, v164, v66
	v_mul_f32_e32 v165, v165, v67
	v_mul_f32_e32 v166, v166, v68
	v_mul_f32_e32 v167, v167, v69
	v_add_co_u32_e32 v172, vcc, 0x30000, v178
	v_cvt_pk_bf16_f32 v168, v160, v161
	v_cvt_pk_bf16_f32 v169, v162, v163
	v_cvt_pk_bf16_f32 v170, v164, v165
	v_cvt_pk_bf16_f32 v171, v166, v167
	v_addc_co_u32_e32 v173, vcc, 0, v179, vcc
	global_store_dwordx4 v[172:173], v[168:171], off
	v_mul_f32_e32 v160, 0xbfb8aa3b, v62
	v_mul_f32_e32 v161, 0xbfb8aa3b, v63
	v_mul_f32_e32 v162, 0xbfb8aa3b, v64
	v_mul_f32_e32 v163, 0xbfb8aa3b, v65
	v_mul_f32_e32 v164, 0xbfb8aa3b, v54
	v_mul_f32_e32 v165, 0xbfb8aa3b, v55
	v_mul_f32_e32 v166, 0xbfb8aa3b, v56
	v_mul_f32_e32 v167, 0xbfb8aa3b, v57
	v_exp_f32_e32 v160, v160
	v_exp_f32_e32 v161, v161
	v_exp_f32_e32 v162, v162
	v_exp_f32_e32 v163, v163
	v_exp_f32_e32 v164, v164
	v_exp_f32_e32 v165, v165
	v_exp_f32_e32 v166, v166
	v_exp_f32_e32 v167, v167
	v_add_f32_e32 v160, 1.0, v160
	v_add_f32_e32 v161, 1.0, v161
	v_add_f32_e32 v162, 1.0, v162
	v_add_f32_e32 v163, 1.0, v163
	v_add_f32_e32 v164, 1.0, v164
	v_add_f32_e32 v165, 1.0, v165
	v_add_f32_e32 v166, 1.0, v166
	v_add_f32_e32 v167, 1.0, v167
	v_rcp_f32_e32 v160, v160
	v_rcp_f32_e32 v161, v161
	v_rcp_f32_e32 v162, v162
	v_rcp_f32_e32 v163, v163
	v_rcp_f32_e32 v164, v164
	v_rcp_f32_e32 v165, v165
	v_rcp_f32_e32 v166, v166
	v_rcp_f32_e32 v167, v167
	v_mul_f32_e32 v160, v62, v160
	v_mul_f32_e32 v161, v63, v161
	v_mul_f32_e32 v162, v64, v162
	v_mul_f32_e32 v163, v65, v163
	v_mul_f32_e32 v164, v54, v164
	v_mul_f32_e32 v165, v55, v165
	v_mul_f32_e32 v166, v56, v166
	v_mul_f32_e32 v167, v57, v167
	v_mul_f32_e32 v160, v160, v58
	v_mul_f32_e32 v161, v161, v59
	v_mul_f32_e32 v162, v162, v60
	v_mul_f32_e32 v163, v163, v61
	v_mul_f32_e32 v164, v164, v50
	v_mul_f32_e32 v165, v165, v51
	v_mul_f32_e32 v166, v166, v52
	v_mul_f32_e32 v167, v167, v53
	v_add_co_u32_e32 v172, vcc, 0x80000, v178
	v_cvt_pk_bf16_f32 v168, v160, v161
	v_cvt_pk_bf16_f32 v169, v162, v163
	v_cvt_pk_bf16_f32 v170, v164, v165
	v_cvt_pk_bf16_f32 v171, v166, v167
	v_addc_co_u32_e32 v173, vcc, 0, v179, vcc
	global_store_dwordx4 v[172:173], v[168:171], off
	v_mul_f32_e32 v160, 0xbfb8aa3b, v46
	v_mul_f32_e32 v161, 0xbfb8aa3b, v47
	v_mul_f32_e32 v162, 0xbfb8aa3b, v48
	v_mul_f32_e32 v163, 0xbfb8aa3b, v49
	v_mul_f32_e32 v164, 0xbfb8aa3b, v38
	v_mul_f32_e32 v165, 0xbfb8aa3b, v39
	v_mul_f32_e32 v166, 0xbfb8aa3b, v40
	v_mul_f32_e32 v167, 0xbfb8aa3b, v41
	v_exp_f32_e32 v160, v160
	v_exp_f32_e32 v161, v161
	v_exp_f32_e32 v162, v162
	v_exp_f32_e32 v163, v163
	v_exp_f32_e32 v164, v164
	v_exp_f32_e32 v165, v165
	v_exp_f32_e32 v166, v166
	v_exp_f32_e32 v167, v167
	v_add_f32_e32 v160, 1.0, v160
	v_add_f32_e32 v161, 1.0, v161
	v_add_f32_e32 v162, 1.0, v162
	v_add_f32_e32 v163, 1.0, v163
	v_add_f32_e32 v164, 1.0, v164
	v_add_f32_e32 v165, 1.0, v165
	v_add_f32_e32 v166, 1.0, v166
	v_add_f32_e32 v167, 1.0, v167
	v_rcp_f32_e32 v160, v160
	v_rcp_f32_e32 v161, v161
	v_rcp_f32_e32 v162, v162
	v_rcp_f32_e32 v163, v163
	v_rcp_f32_e32 v164, v164
	v_rcp_f32_e32 v165, v165
	v_rcp_f32_e32 v166, v166
	v_rcp_f32_e32 v167, v167
	v_mul_f32_e32 v160, v46, v160
	v_mul_f32_e32 v161, v47, v161
	v_mul_f32_e32 v162, v48, v162
	v_mul_f32_e32 v163, v49, v163
	v_mul_f32_e32 v164, v38, v164
	v_mul_f32_e32 v165, v39, v165
	v_mul_f32_e32 v166, v40, v166
	v_mul_f32_e32 v167, v41, v167
	v_mul_f32_e32 v160, v160, v42
	v_mul_f32_e32 v161, v161, v43
	v_mul_f32_e32 v162, v162, v44
	v_mul_f32_e32 v163, v163, v45
	v_mul_f32_e32 v164, v164, v34
	v_mul_f32_e32 v165, v165, v35
	v_mul_f32_e32 v166, v166, v36
	v_mul_f32_e32 v167, v167, v37
	v_add_co_u32_e32 v172, vcc, 0x90000, v178
	v_cvt_pk_bf16_f32 v168, v160, v161
	v_cvt_pk_bf16_f32 v169, v162, v163
	v_cvt_pk_bf16_f32 v170, v164, v165
	v_cvt_pk_bf16_f32 v171, v166, v167
	v_addc_co_u32_e32 v173, vcc, 0, v179, vcc
	global_store_dwordx4 v[172:173], v[168:171], off
	v_mul_f32_e32 v160, 0xbfb8aa3b, v30
	v_mul_f32_e32 v161, 0xbfb8aa3b, v31
	v_mul_f32_e32 v162, 0xbfb8aa3b, v32
	v_mul_f32_e32 v163, 0xbfb8aa3b, v33
	v_mul_f32_e32 v164, 0xbfb8aa3b, v22
	v_mul_f32_e32 v165, 0xbfb8aa3b, v23
	v_mul_f32_e32 v166, 0xbfb8aa3b, v24
	v_mul_f32_e32 v167, 0xbfb8aa3b, v25
	v_exp_f32_e32 v160, v160
	v_exp_f32_e32 v161, v161
	v_exp_f32_e32 v162, v162
	v_exp_f32_e32 v163, v163
	v_exp_f32_e32 v164, v164
	v_exp_f32_e32 v165, v165
	v_exp_f32_e32 v166, v166
	v_exp_f32_e32 v167, v167
	v_add_f32_e32 v160, 1.0, v160
	v_add_f32_e32 v161, 1.0, v161
	v_add_f32_e32 v162, 1.0, v162
	v_add_f32_e32 v163, 1.0, v163
	v_add_f32_e32 v164, 1.0, v164
	v_add_f32_e32 v165, 1.0, v165
	v_add_f32_e32 v166, 1.0, v166
	v_add_f32_e32 v167, 1.0, v167
	v_rcp_f32_e32 v160, v160
	v_rcp_f32_e32 v161, v161
	v_rcp_f32_e32 v162, v162
	v_rcp_f32_e32 v163, v163
	v_rcp_f32_e32 v164, v164
	v_rcp_f32_e32 v165, v165
	v_rcp_f32_e32 v166, v166
	v_rcp_f32_e32 v167, v167
	v_mul_f32_e32 v160, v30, v160
	v_mul_f32_e32 v161, v31, v161
	v_mul_f32_e32 v162, v32, v162
	v_mul_f32_e32 v163, v33, v163
	v_mul_f32_e32 v164, v22, v164
	v_mul_f32_e32 v165, v23, v165
	v_mul_f32_e32 v166, v24, v166
	v_mul_f32_e32 v167, v25, v167
	v_mul_f32_e32 v160, v160, v26
	v_mul_f32_e32 v161, v161, v27
	v_mul_f32_e32 v162, v162, v28
	v_mul_f32_e32 v163, v163, v29
	v_mul_f32_e32 v164, v164, v18
	v_mul_f32_e32 v165, v165, v19
	v_mul_f32_e32 v166, v166, v20
	v_mul_f32_e32 v167, v167, v21
	v_add_co_u32_e32 v172, vcc, 0xa0000, v178
	v_cvt_pk_bf16_f32 v168, v160, v161
	v_cvt_pk_bf16_f32 v169, v162, v163
	v_cvt_pk_bf16_f32 v170, v164, v165
	v_cvt_pk_bf16_f32 v171, v166, v167
	v_addc_co_u32_e32 v173, vcc, 0, v179, vcc
	global_store_dwordx4 v[172:173], v[168:171], off
	v_mul_f32_e32 v160, 0xbfb8aa3b, v14
	v_mul_f32_e32 v161, 0xbfb8aa3b, v15
	v_mul_f32_e32 v162, 0xbfb8aa3b, v16
	v_mul_f32_e32 v163, 0xbfb8aa3b, v17
	v_mul_f32_e32 v164, 0xbfb8aa3b, v6
	v_mul_f32_e32 v165, 0xbfb8aa3b, v7
	v_mul_f32_e32 v166, 0xbfb8aa3b, v8
	v_mul_f32_e32 v167, 0xbfb8aa3b, v9
	v_exp_f32_e32 v160, v160
	v_exp_f32_e32 v161, v161
	v_exp_f32_e32 v162, v162
	v_exp_f32_e32 v163, v163
	v_exp_f32_e32 v164, v164
	v_exp_f32_e32 v165, v165
	v_exp_f32_e32 v166, v166
	v_exp_f32_e32 v167, v167
	v_add_f32_e32 v160, 1.0, v160
	v_add_f32_e32 v161, 1.0, v161
	v_add_f32_e32 v162, 1.0, v162
	v_add_f32_e32 v163, 1.0, v163
	v_add_f32_e32 v164, 1.0, v164
	v_add_f32_e32 v165, 1.0, v165
	v_add_f32_e32 v166, 1.0, v166
	v_add_f32_e32 v167, 1.0, v167
	v_rcp_f32_e32 v160, v160
	v_rcp_f32_e32 v161, v161
	v_rcp_f32_e32 v162, v162
	v_rcp_f32_e32 v163, v163
	v_rcp_f32_e32 v164, v164
	v_rcp_f32_e32 v165, v165
	v_rcp_f32_e32 v166, v166
	v_rcp_f32_e32 v167, v167
	v_mul_f32_e32 v160, v14, v160
	v_mul_f32_e32 v161, v15, v161
	v_mul_f32_e32 v162, v16, v162
	v_mul_f32_e32 v163, v17, v163
	v_mul_f32_e32 v164, v6, v164
	v_mul_f32_e32 v165, v7, v165
	v_mul_f32_e32 v166, v8, v166
	v_mul_f32_e32 v167, v9, v167
	v_mul_f32_e32 v160, v160, v10
	v_mul_f32_e32 v161, v161, v11
	v_mul_f32_e32 v162, v162, v12
	v_mul_f32_e32 v163, v163, v13
	v_mul_f32_e32 v164, v164, v2
	v_mul_f32_e32 v165, v165, v3
	v_mul_f32_e32 v166, v166, v4
	v_mul_f32_e32 v167, v167, v5
	v_add_co_u32_e32 v172, vcc, 0xb0000, v178
	v_cvt_pk_bf16_f32 v168, v160, v161
	v_cvt_pk_bf16_f32 v169, v162, v163
	v_cvt_pk_bf16_f32 v170, v164, v165
	v_cvt_pk_bf16_f32 v171, v166, v167
	v_addc_co_u32_e32 v173, vcc, 0, v179, vcc
	global_store_dwordx4 v[172:173], v[168:171], off
	s_mov_b64 s[0:1], -1
	s_and_b64 vcc, exec, s[2:3]
	s_cbranch_vccnz .LBB0_1322
	s_andn2_b64 vcc, exec, s[4:5]
	v_mov_b32 v2, 0
	s_cbranch_vccnz .LBB0_1321
	s_barrier
	s_branch .LBB0_1321
